# attention epilogue: 8 dwordx2 stores widened to 4 dwordx4 via v_permlane32_swap (strategy 7.3), on top of u10_v2_rope
# speedup vs baseline: 1.0003x; 1.0003x over previous
.LBB0_1109:
	s_setprio 0
	s_nop 1
	v_mov_b32_e32 v4, v224
	s_nop 1
	v_permlane32_swap_b32_e32 v224, v4
	v_add_f32_e32 v4, v224, v4
	v_div_scale_f32 v5, s[0:1], v4, v4, 1.0
	v_rcp_f32_e32 v6, v5
	s_lshl_b32 s30, s35, 7
	v_mov_b32_e32 v199, v3
	s_mov_b64 s[0:1], 0x1701b400
	v_fma_f32 v7, -v5, v6, 1.0
	v_fmac_f32_e32 v6, v7, v6
	v_div_scale_f32 v7, vcc, 1.0, v4, 1.0
	v_mul_f32_e32 v8, v7, v6
	v_fma_f32 v9, -v5, v8, v7
	v_fmac_f32_e32 v8, v9, v6
	v_fma_f32 v5, -v5, v8, v7
	v_div_fmas_f32 v5, v5, v6, v8
	v_lshlrev_b64 v[6:7], 11, v[200:201]
	v_lshl_add_u64 v[6:7], s[44:45], 0, v[6:7]
	v_lshl_add_u64 v[6:7], v[6:7], 0, s[30:31]
	v_lshl_add_u64 v[6:7], v[6:7], 0, v[198:199]
	v_div_fixup_f32 v4, v5, v4, 1.0
	v_lshl_add_u64 v[8:9], v[6:7], 0, s[0:1]
	v_mbcnt_lo_u32_b32 v6, -1, 0
	v_mbcnt_hi_u32_b32 v6, -1, v6
	v_and_b32_e32 v6, 32, v6
	v_lshrrev_b32_e32 v6, 2, v6
	v_mov_b32_e32 v7, 0
	v_lshl_add_u64 v[8:9], v[8:9], 0, v[6:7]
	v_pk_mul_f32 v[10:11], v[36:37], v[4:5] op_sel_hi:[1,0]
	v_pk_mul_f32 v[12:13], v[38:39], v[4:5] op_sel_hi:[1,0]
	v_pk_mul_f32 v[14:15], v[40:41], v[4:5] op_sel_hi:[1,0]
	v_pk_mul_f32 v[16:17], v[42:43], v[4:5] op_sel_hi:[1,0]
	v_cvt_pk_bf16_f32 v20, v10, v11
	v_cvt_pk_bf16_f32 v21, v12, v13
	v_cvt_pk_bf16_f32 v22, v14, v15
	v_cvt_pk_bf16_f32 v23, v16, v17
	s_nop 1
	v_permlane32_swap_b32_e32 v20, v22
	v_permlane32_swap_b32_e32 v21, v23
	global_store_dwordx4 v[8:9], v[20:23], off
	v_pk_mul_f32 v[10:11], v[44:45], v[4:5] op_sel_hi:[1,0]
	v_pk_mul_f32 v[12:13], v[46:47], v[4:5] op_sel_hi:[1,0]
	v_pk_mul_f32 v[14:15], v[48:49], v[4:5] op_sel_hi:[1,0]
	v_pk_mul_f32 v[16:17], v[50:51], v[4:5] op_sel_hi:[1,0]
	v_cvt_pk_bf16_f32 v24, v10, v11
	v_cvt_pk_bf16_f32 v25, v12, v13
	v_cvt_pk_bf16_f32 v26, v14, v15
	v_cvt_pk_bf16_f32 v27, v16, v17
	s_nop 1
	v_permlane32_swap_b32_e32 v24, v26
	v_permlane32_swap_b32_e32 v25, v27
	global_store_dwordx4 v[8:9], v[24:27], off offset:32
	v_pk_mul_f32 v[10:11], v[52:53], v[4:5] op_sel_hi:[1,0]
	v_pk_mul_f32 v[12:13], v[54:55], v[4:5] op_sel_hi:[1,0]
	v_pk_mul_f32 v[14:15], v[56:57], v[4:5] op_sel_hi:[1,0]
	v_pk_mul_f32 v[16:17], v[58:59], v[4:5] op_sel_hi:[1,0]
	v_cvt_pk_bf16_f32 v28, v10, v11
	v_cvt_pk_bf16_f32 v29, v12, v13
	v_cvt_pk_bf16_f32 v30, v14, v15
	v_cvt_pk_bf16_f32 v31, v16, v17
	s_nop 1
	v_permlane32_swap_b32_e32 v28, v30
	v_permlane32_swap_b32_e32 v29, v31
	global_store_dwordx4 v[8:9], v[28:31], off offset:64
	v_pk_mul_f32 v[10:11], v[60:61], v[4:5] op_sel_hi:[1,0]
	v_pk_mul_f32 v[12:13], v[62:63], v[4:5] op_sel_hi:[1,0]
	v_pk_mul_f32 v[14:15], v[64:65], v[4:5] op_sel_hi:[1,0]
	v_pk_mul_f32 v[16:17], v[66:67], v[4:5] op_sel_hi:[1,0]
	v_cvt_pk_bf16_f32 v32, v10, v11
	v_cvt_pk_bf16_f32 v33, v12, v13
	v_cvt_pk_bf16_f32 v34, v14, v15
	v_cvt_pk_bf16_f32 v35, v16, v17
	s_nop 1
	v_permlane32_swap_b32_e32 v32, v34
	v_permlane32_swap_b32_e32 v33, v35
	global_store_dwordx4 v[8:9], v[32:35], off offset:96
	v_readlane_b32 s0, v254, 4
	v_readlane_b32 s1, v254, 5
	s_load_dword s0, s[0:1], 0x0
	s_waitcnt lgkmcnt(0)
	s_add_i32 s15, s0, s15
	s_cmp_lt_i32 s15, s14
	s_cbranch_scc0 .LBB0_1140
